# grid barrier: workgroups that are not last in their XCD wait on the top-level generation word directly (equal to the per-XCD generation); the per-XCD republish atomic is dropped
# speedup vs baseline: 1.0031x; 1.0031x over previous
.LBB0_64:
	v_readlane_b32 s4, v253, 2
	s_lshl_b32 s4, s4, 8
	s_add_u32 s4, s88, s4
	s_addc_u32 s5, s89, 0
	v_mov_b32_e32 v2, 0x1000
	v_mov_b32_e32 v4, 1
	global_atomic_add v4, v2, v4, s[4:5] offset:1024 sc0
	v_cvt_f32_u32_e32 v2, v3
	v_sub_u32_e32 v5, 0, v3
	v_rcp_iflag_f32_e32 v2, v2
	s_nop 0
	v_mul_f32_e32 v2, 0x4f7ffffe, v2
	v_cvt_u32_f32_e32 v2, v2
	v_mul_lo_u32 v5, v5, v2
	v_mul_hi_u32 v5, v2, v5
	v_add_u32_e32 v2, v2, v5
	s_waitcnt vmcnt(0)
	v_mul_hi_u32 v2, v4, v2
	v_mul_lo_u32 v5, v2, v3
	v_sub_u32_e32 v5, v4, v5
	v_add_u32_e32 v6, 1, v2
	v_cmp_ge_u32_e32 vcc, v5, v3
	v_add_u32_e32 v4, 1, v4
	s_nop 0
	v_cndmask_b32_e32 v2, v2, v6, vcc
	v_sub_u32_e32 v6, v5, v3
	v_cndmask_b32_e32 v5, v5, v6, vcc
	v_add_u32_e32 v6, 1, v2
	v_cmp_ge_u32_e32 vcc, v5, v3
	s_nop 1
	v_cndmask_b32_e32 v2, v2, v6, vcc
	v_mul_lo_u32 v5, v3, v2
	v_add_u32_e32 v3, v5, v3
	v_cmp_ne_u32_e32 vcc, v4, v3
	s_and_saveexec_b64 s[6:7], vcc
	s_xor_b64 s[6:7], exec, s[6:7]
	s_cbranch_execz .LBB0_78
	s_waitcnt lgkmcnt(0)
	v_mov_b32_e32 v1, 0x3100
	global_load_dword v1, v1, s[88:89] offset:1024 sc1
	s_add_u32 s10, s88, 0x3500
	s_addc_u32 s11, s89, 0
	s_waitcnt vmcnt(0)
	v_cmp_eq_u32_e32 vcc, v1, v2
	s_and_saveexec_b64 s[8:9], vcc
	s_cbranch_execz .LBB0_77
	s_mov_b32 s30, 1
	s_mov_b64 s[14:15], 0
	v_mov_b32_e32 v1, 0
	s_branch .LBB0_68

.LBB0_95:
	s_or_b64 exec, exec, s[6:7]
	v_mov_b32_e32 v1, 0x2000
	v_mov_b32_e32 v2, 1
	s_waitcnt vmcnt(0)
	buffer_inv sc1
	s_waitcnt vmcnt(0)

.LBB0_186:
	v_readlane_b32 s4, v253, 2
	s_lshl_b32 s4, s4, 8
	s_add_u32 s4, s88, s4
	s_addc_u32 s5, s89, 0
	v_mov_b32_e32 v3, 0x1000
	v_mov_b32_e32 v5, 1
	global_atomic_add v5, v3, v5, s[4:5] offset:1024 sc0
	v_cvt_f32_u32_e32 v3, v4
	v_sub_u32_e32 v6, 0, v4
	v_rcp_iflag_f32_e32 v3, v3
	s_nop 0
	v_mul_f32_e32 v3, 0x4f7ffffe, v3
	v_cvt_u32_f32_e32 v3, v3
	v_mul_lo_u32 v6, v6, v3
	v_mul_hi_u32 v6, v3, v6
	v_add_u32_e32 v3, v3, v6
	s_waitcnt vmcnt(0)
	v_mul_hi_u32 v3, v5, v3
	v_mul_lo_u32 v6, v3, v4
	v_sub_u32_e32 v6, v5, v6
	v_add_u32_e32 v7, 1, v3
	v_cmp_ge_u32_e32 vcc, v6, v4
	v_add_u32_e32 v5, 1, v5
	s_nop 0
	v_cndmask_b32_e32 v3, v3, v7, vcc
	v_sub_u32_e32 v7, v6, v4
	v_cndmask_b32_e32 v6, v6, v7, vcc
	v_add_u32_e32 v7, 1, v3
	v_cmp_ge_u32_e32 vcc, v6, v4
	s_nop 1
	v_cndmask_b32_e32 v3, v3, v7, vcc
	v_mul_lo_u32 v6, v4, v3
	v_add_u32_e32 v4, v6, v4
	v_cmp_ne_u32_e32 vcc, v5, v4
	s_and_saveexec_b64 s[6:7], vcc
	s_xor_b64 s[6:7], exec, s[6:7]
	s_cbranch_execz .LBB0_200
	s_waitcnt lgkmcnt(0)
	v_mov_b32_e32 v2, 0x3100
	global_load_dword v2, v2, s[88:89] offset:1024 sc1
	s_add_u32 s10, s88, 0x3500
	s_addc_u32 s11, s89, 0
	s_waitcnt vmcnt(0)
	v_cmp_eq_u32_e32 vcc, v2, v3
	s_and_saveexec_b64 s[8:9], vcc
	s_cbranch_execz .LBB0_199
	s_mov_b32 s24, 1
	s_mov_b64 s[14:15], 0
	v_mov_b32_e32 v2, 0
	s_branch .LBB0_190

.LBB0_217:
	s_or_b64 exec, exec, s[6:7]
	v_mov_b32_e32 v2, 0x2000
	v_mov_b32_e32 v3, 1
	s_waitcnt vmcnt(0)
	buffer_inv sc1
	s_waitcnt vmcnt(0)

.LBB0_405:
	v_readlane_b32 s4, v253, 2
	s_lshl_b32 s4, s4, 8
	s_add_u32 s4, s88, s4
	s_addc_u32 s5, s89, 0
	v_mov_b32_e32 v2, 0x1000
	v_mov_b32_e32 v4, 1
	global_atomic_add v4, v2, v4, s[4:5] offset:1024 sc0
	v_cvt_f32_u32_e32 v2, v3
	v_sub_u32_e32 v5, 0, v3
	v_rcp_iflag_f32_e32 v2, v2
	s_nop 0
	v_mul_f32_e32 v2, 0x4f7ffffe, v2
	v_cvt_u32_f32_e32 v2, v2
	v_mul_lo_u32 v5, v5, v2
	v_mul_hi_u32 v5, v2, v5
	v_add_u32_e32 v2, v2, v5
	s_waitcnt vmcnt(0)
	v_mul_hi_u32 v2, v4, v2
	v_mul_lo_u32 v5, v2, v3
	v_sub_u32_e32 v5, v4, v5
	v_add_u32_e32 v6, 1, v2
	v_cmp_ge_u32_e32 vcc, v5, v3
	v_add_u32_e32 v4, 1, v4
	s_nop 0
	v_cndmask_b32_e32 v2, v2, v6, vcc
	v_sub_u32_e32 v6, v5, v3
	v_cndmask_b32_e32 v5, v5, v6, vcc
	v_add_u32_e32 v6, 1, v2
	v_cmp_ge_u32_e32 vcc, v5, v3
	s_nop 1
	v_cndmask_b32_e32 v2, v2, v6, vcc
	v_mul_lo_u32 v5, v3, v2
	v_add_u32_e32 v3, v5, v3
	v_cmp_ne_u32_e32 vcc, v4, v3
	s_and_saveexec_b64 s[6:7], vcc
	s_xor_b64 s[6:7], exec, s[6:7]
	s_cbranch_execz .LBB0_419
	s_waitcnt lgkmcnt(0)
	v_mov_b32_e32 v1, 0x3100
	global_load_dword v1, v1, s[88:89] offset:1024 sc1
	s_add_u32 s10, s88, 0x3500
	s_addc_u32 s11, s89, 0
	s_waitcnt vmcnt(0)
	v_cmp_eq_u32_e32 vcc, v1, v2
	s_and_saveexec_b64 s[8:9], vcc
	s_cbranch_execz .LBB0_418
	s_mov_b32 s24, 1
	s_mov_b64 s[14:15], 0
	v_mov_b32_e32 v1, 0
	s_branch .LBB0_409

.LBB0_800:
	v_readlane_b32 s4, v253, 2
	s_lshl_b32 s4, s4, 8
	s_add_u32 s4, s88, s4
	s_addc_u32 s5, s89, 0
	v_mov_b32_e32 v2, 0x1000
	v_mov_b32_e32 v4, 1
	global_atomic_add v4, v2, v4, s[4:5] offset:1024 sc0
	v_cvt_f32_u32_e32 v2, v3
	v_sub_u32_e32 v5, 0, v3
	v_rcp_iflag_f32_e32 v2, v2
	s_nop 0
	v_mul_f32_e32 v2, 0x4f7ffffe, v2
	v_cvt_u32_f32_e32 v2, v2
	v_mul_lo_u32 v5, v5, v2
	v_mul_hi_u32 v5, v2, v5
	v_add_u32_e32 v2, v2, v5
	s_waitcnt vmcnt(0)
	v_mul_hi_u32 v2, v4, v2
	v_mul_lo_u32 v5, v2, v3
	v_sub_u32_e32 v5, v4, v5
	v_add_u32_e32 v6, 1, v2
	v_cmp_ge_u32_e32 vcc, v5, v3
	v_add_u32_e32 v4, 1, v4
	s_nop 0
	v_cndmask_b32_e32 v2, v2, v6, vcc
	v_sub_u32_e32 v6, v5, v3
	v_cndmask_b32_e32 v5, v5, v6, vcc
	v_add_u32_e32 v6, 1, v2
	v_cmp_ge_u32_e32 vcc, v5, v3
	s_nop 1
	v_cndmask_b32_e32 v2, v2, v6, vcc
	v_mul_lo_u32 v5, v3, v2
	v_add_u32_e32 v3, v5, v3
	v_cmp_ne_u32_e32 vcc, v4, v3
	s_and_saveexec_b64 s[6:7], vcc
	s_xor_b64 s[6:7], exec, s[6:7]
	s_cbranch_execz .LBB0_814
	s_waitcnt lgkmcnt(0)
	v_mov_b32_e32 v1, 0x3100
	global_load_dword v1, v1, s[88:89] offset:1024 sc1
	s_add_u32 s10, s88, 0x3500
	s_addc_u32 s11, s89, 0
	s_waitcnt vmcnt(0)
	v_cmp_eq_u32_e32 vcc, v1, v2
	s_and_saveexec_b64 s[8:9], vcc
	s_cbranch_execz .LBB0_813
	s_mov_b32 s22, 1
	s_mov_b64 s[12:13], 0
	v_mov_b32_e32 v1, 0
	s_branch .LBB0_804

.LBB0_1002:
	v_readlane_b32 s2, v253, 2
	s_lshl_b32 s2, s2, 8
	s_add_u32 s2, s88, s2
	s_addc_u32 s3, s89, 0
	v_mov_b32_e32 v2, 0x1000
	v_mov_b32_e32 v4, 1
	global_atomic_add v4, v2, v4, s[2:3] offset:1024 sc0
	v_cvt_f32_u32_e32 v2, v3
	v_sub_u32_e32 v5, 0, v3
	v_rcp_iflag_f32_e32 v2, v2
	s_nop 0
	v_mul_f32_e32 v2, 0x4f7ffffe, v2
	v_cvt_u32_f32_e32 v2, v2
	v_mul_lo_u32 v5, v5, v2
	v_mul_hi_u32 v5, v2, v5
	v_add_u32_e32 v2, v2, v5
	s_waitcnt vmcnt(0)
	v_mul_hi_u32 v2, v4, v2
	v_mul_lo_u32 v5, v2, v3
	v_sub_u32_e32 v5, v4, v5
	v_add_u32_e32 v6, 1, v2
	v_cmp_ge_u32_e32 vcc, v5, v3
	v_add_u32_e32 v4, 1, v4
	s_nop 0
	v_cndmask_b32_e32 v2, v2, v6, vcc
	v_sub_u32_e32 v6, v5, v3
	v_cndmask_b32_e32 v5, v5, v6, vcc
	v_add_u32_e32 v6, 1, v2
	v_cmp_ge_u32_e32 vcc, v5, v3
	s_nop 1
	v_cndmask_b32_e32 v2, v2, v6, vcc
	v_mul_lo_u32 v5, v3, v2
	v_add_u32_e32 v3, v5, v3
	v_cmp_ne_u32_e32 vcc, v4, v3
	s_and_saveexec_b64 s[4:5], vcc
	s_xor_b64 s[4:5], exec, s[4:5]
	s_cbranch_execz .LBB0_1016
	s_waitcnt lgkmcnt(0)
	v_mov_b32_e32 v1, 0x3100
	global_load_dword v1, v1, s[88:89] offset:1024 sc1
	s_add_u32 s8, s88, 0x3500
	s_addc_u32 s9, s89, 0
	s_waitcnt vmcnt(0)
	v_cmp_eq_u32_e32 vcc, v1, v2
	s_and_saveexec_b64 s[6:7], vcc
	s_cbranch_execz .LBB0_1015
	s_mov_b32 s20, 1
	s_mov_b64 s[10:11], 0
	v_mov_b32_e32 v1, 0
	s_branch .LBB0_1006

.LBB0_1033:
	s_or_b64 exec, exec, s[4:5]
	v_mov_b32_e32 v1, 0x2000
	v_mov_b32_e32 v2, 1
	s_waitcnt vmcnt(0)
	buffer_inv sc1
	s_waitcnt vmcnt(0)

.LBB0_1223:
	v_readlane_b32 s2, v253, 2
	s_lshl_b32 s2, s2, 8
	s_add_u32 s2, s88, s2
	s_addc_u32 s3, s89, 0
	v_mov_b32_e32 v1, 0x1000
	v_mov_b32_e32 v3, 1
	global_atomic_add v3, v1, v3, s[2:3] offset:1024 sc0
	v_cvt_f32_u32_e32 v1, v2
	v_sub_u32_e32 v4, 0, v2
	v_rcp_iflag_f32_e32 v1, v1
	s_nop 0
	v_mul_f32_e32 v1, 0x4f7ffffe, v1
	v_cvt_u32_f32_e32 v1, v1
	v_mul_lo_u32 v4, v4, v1
	v_mul_hi_u32 v4, v1, v4
	v_add_u32_e32 v1, v1, v4
	s_waitcnt vmcnt(0)
	v_mul_hi_u32 v1, v3, v1
	v_mul_lo_u32 v4, v1, v2
	v_sub_u32_e32 v4, v3, v4
	v_add_u32_e32 v5, 1, v1
	v_cmp_ge_u32_e32 vcc, v4, v2
	v_add_u32_e32 v3, 1, v3
	s_nop 0
	v_cndmask_b32_e32 v1, v1, v5, vcc
	v_sub_u32_e32 v5, v4, v2
	v_cndmask_b32_e32 v4, v4, v5, vcc
	v_add_u32_e32 v5, 1, v1
	v_cmp_ge_u32_e32 vcc, v4, v2
	s_nop 1
	v_cndmask_b32_e32 v1, v1, v5, vcc
	v_mul_lo_u32 v4, v2, v1
	v_add_u32_e32 v2, v4, v2
	v_cmp_ne_u32_e32 vcc, v3, v2
	s_and_saveexec_b64 s[4:5], vcc
	s_xor_b64 s[4:5], exec, s[4:5]
	s_cbranch_execz .LBB0_1237
	s_waitcnt lgkmcnt(0)
	v_mov_b32_e32 v0, 0x3100
	global_load_dword v0, v0, s[88:89] offset:1024 sc1
	s_add_u32 s8, s88, 0x3500
	s_addc_u32 s9, s89, 0
	s_waitcnt vmcnt(0)
	v_cmp_eq_u32_e32 vcc, v0, v1
	s_and_saveexec_b64 s[6:7], vcc
	s_cbranch_execz .LBB0_1236
	s_mov_b32 s20, 1
	s_mov_b64 s[10:11], 0
	v_mov_b32_e32 v0, 0
	s_branch .LBB0_1227

.LBB0_1254:
	s_or_b64 exec, exec, s[4:5]
	v_mov_b32_e32 v0, 0x2000
	v_mov_b32_e32 v1, 1
	s_waitcnt vmcnt(0)
	buffer_inv sc1
	s_waitcnt vmcnt(0)
